# s11 + exact dead-tile shortcut in 4 mask sites: a wave whose whole tile is masked writes p=0, skips the row-max chain and the 32 exps
# baseline (speedup 1.0000x reference)
; __device__ __forceinline__ void cmask(f32x16& p0, f32x16& p1, int jb, int qrel, int hi) {
;     const float NEG = -INFINITY; int kb = 64 * jb + 4 * hi;
; #pragma unroll
;     for (int r = 0; r < 16; ++r) { int kv = kb + (r & 3) + 8 * (r >> 2); if (kv > qrel) p0[r] = NEG; if (kv + 32 > qrel) p1[r] = NEG; }
; }
.LBB0_477:
	v_add_u32_e32 v184, s0, v230
	ds_read_b64_tr_b16 v[180:181], v184 offset:24576
	ds_read_b64_tr_b16 v[182:183], v184 offset:25088
	s_waitcnt lgkmcnt(9)
	v_mfma_f32_32x32x16_f16 v[48:63], v[176:179], v[128:131], v[48:63]
	v_add_f32_e32 v132, v80, v81
	v_add_f32_e32 v132, v82, v132
	v_add_f32_e32 v132, v83, v132
	v_add_f32_e32 v132, v84, v132
	v_add_f32_e32 v132, v85, v132
	v_cvt_pk_f16_f32 v144, v80, v81
	v_cvt_pk_f16_f32 v145, v82, v83
	ds_read_b64_tr_b16 v[176:177], v184 offset:28672
	ds_read_b64_tr_b16 v[178:179], v184 offset:29184
	s_waitcnt lgkmcnt(10)
	v_mfma_f32_32x32x16_f16 v[32:47], v[172:175], v[128:131], v[32:47]
	v_add_f32_e32 v80, v86, v132
	v_add_f32_e32 v80, v87, v80
	v_add_f32_e32 v80, v88, v80
	v_add_f32_e32 v80, v89, v80
	v_cvt_pk_f16_f32 v146, v84, v85
	v_cvt_pk_f16_f32 v147, v86, v87
	ds_read_b64_tr_b16 v[172:173], v184 offset:25600
	ds_read_b64_tr_b16 v[174:175], v184 offset:26112
	s_waitcnt lgkmcnt(11)
	v_mfma_f32_32x32x16_f16 v[48:63], v[168:171], v[124:127], v[48:63]
	v_add_f32_e32 v80, v90, v80
	v_add_f32_e32 v80, v91, v80
	v_add_f32_e32 v80, v92, v80
	v_add_f32_e32 v80, v93, v80
	v_cvt_pk_f16_f32 v140, v88, v89
	v_cvt_pk_f16_f32 v141, v90, v91
	ds_read_b64_tr_b16 v[84:85], v184 offset:29696
	ds_read_b64_tr_b16 v[86:87], v184 offset:30208
	s_waitcnt lgkmcnt(12)
	v_mfma_f32_32x32x16_f16 v[32:47], v[164:167], v[124:127], v[32:47]
	v_add_f32_e32 v80, v94, v80
	v_add_f32_e32 v80, v95, v80
	v_add_f32_e32 v80, v64, v80
	v_add_f32_e32 v88, v65, v80
	v_cvt_pk_f16_f32 v142, v92, v93
	v_cvt_pk_f16_f32 v143, v94, v95
	ds_read_b64_tr_b16 v[80:81], v184 offset:26624
	ds_read_b64_tr_b16 v[82:83], v184 offset:27136
	s_waitcnt lgkmcnt(13)
	v_mfma_f32_32x32x16_f16 v[48:63], v[160:163], v[120:123], v[48:63]
	v_add_f32_e32 v88, v66, v88
	v_add_f32_e32 v88, v67, v88
	v_add_f32_e32 v88, v68, v88
	v_add_f32_e32 v88, v69, v88
	v_cvt_pk_f16_f32 v136, v64, v65
	v_cvt_pk_f16_f32 v137, v66, v67
	ds_read_b64_tr_b16 v[160:161], v184 offset:30720
	ds_read_b64_tr_b16 v[162:163], v184 offset:31232
	s_waitcnt lgkmcnt(14)
	v_mfma_f32_32x32x16_f16 v[32:47], v[152:155], v[120:123], v[32:47]
	v_add_f32_e32 v64, v70, v88
	v_add_f32_e32 v64, v71, v64
	v_add_f32_e32 v64, v72, v64
	v_add_f32_e32 v88, v73, v64
	v_cvt_pk_f16_f32 v138, v68, v69
	v_cvt_pk_f16_f32 v139, v70, v71
	ds_read_b64_tr_b16 v[64:65], v184 offset:27648
	ds_read_b64_tr_b16 v[66:67], v184 offset:28160
	s_waitcnt lgkmcnt(14)
	v_mfma_f32_32x32x16_f16 v[48:63], v[156:159], v[116:119], v[48:63]
	v_add_f32_e32 v68, v74, v88
	v_add_f32_e32 v68, v75, v68
	v_add_f32_e32 v68, v76, v68
	v_add_f32_e32 v68, v77, v68
	v_cvt_pk_f16_f32 v132, v72, v73
	v_cvt_pk_f16_f32 v133, v74, v75
	ds_read_b64_tr_b16 v[152:153], v184 offset:31744
	ds_read_b64_tr_b16 v[154:155], v184 offset:32256
	v_mfma_f32_32x32x16_f16 v[32:47], v[148:151], v[116:119], v[32:47]
	v_add_f32_e32 v68, v78, v68
	v_add_f32_e32 v68, v79, v68
	v_add_f32_e32 v68, 0, v68
	v_cvt_pk_f16_f32 v134, v76, v77
	v_cvt_pk_f16_f32 v135, v78, v79
	s_add_i32 s0, s70, s89
	s_cmp_lt_u32 s69, 3
	s_cselect_b64 s[40:41], -1, 0
	s_mov_b32 s1, m0
	s_mov_b32 m0, s0
	s_nop 0
	global_load_lds_dwordx4 v[194:195], off
	s_mov_b32 m0, s1
	s_and_b64 s[0:1], s[40:41], exec
	s_cselect_b32 s18, s50, -3
	s_add_i32 s18, s18, s69
	v_mad_i64_i32 v[70:71], s[0:1], s18, v249, v[216:217]
	s_add_i32 s0, s68, s36
	s_mov_b32 s1, m0
	s_mov_b32 m0, s0
	s_nop 0
	global_load_lds_dwordx4 v[70:71], off
	s_mov_b32 m0, s1
	s_cmp_gt_u32 s69, 3
	s_cbranch_scc1 .LBB0_479
	s_mov_b64 s[100:101], exec
	v_sub_u32_e32 v70, v215, v197
	v_add_u32_e32 v70, 0x7b, v70
	v_cmp_gt_i32_e32 vcc, 0, v70
	s_cmp_eq_u64 vcc, exec
	s_cbranch_scc1 .Lmask_dead_9
	v_cmpx_gt_i32_e32 59, v70
	s_nop 3
	s_cbranch_execz .Lmaskx_done_9
	v_mov_b32_e32 v47, v248
	v_cmpx_gt_i32_e32 58, v70
	v_mov_b32_e32 v46, v248
	v_cmpx_gt_i32_e32 57, v70
	v_mov_b32_e32 v45, v248
	v_cmpx_gt_i32_e32 56, v70
	v_mov_b32_e32 v44, v248
	v_cmpx_gt_i32_e32 51, v70
	v_mov_b32_e32 v43, v248
	v_cmpx_gt_i32_e32 50, v70
	v_mov_b32_e32 v42, v248
	v_cmpx_gt_i32_e32 49, v70
	v_mov_b32_e32 v41, v248
	v_cmpx_gt_i32_e32 48, v70
	v_mov_b32_e32 v40, v248
	v_cmpx_gt_i32_e32 43, v70
	v_mov_b32_e32 v39, v248
	v_cmpx_gt_i32_e32 42, v70
	v_mov_b32_e32 v38, v248
	v_cmpx_gt_i32_e32 41, v70
	v_mov_b32_e32 v37, v248
	v_cmpx_gt_i32_e32 40, v70
	v_mov_b32_e32 v36, v248
	v_cmpx_gt_i32_e32 35, v70
	v_mov_b32_e32 v35, v248
	v_cmpx_gt_i32_e32 34, v70
	v_mov_b32_e32 v34, v248
	v_cmpx_gt_i32_e32 33, v70
	v_mov_b32_e32 v33, v248
	v_cmpx_gt_i32_e32 32, v70
	v_mov_b32_e32 v32, v248
	v_cmpx_gt_i32_e32 27, v70
	v_mov_b32_e32 v63, v248
	v_cmpx_gt_i32_e32 26, v70
	v_mov_b32_e32 v62, v248
	v_cmpx_gt_i32_e32 25, v70
	v_mov_b32_e32 v61, v248
	v_cmpx_gt_i32_e32 24, v70
	v_mov_b32_e32 v60, v248
	v_cmpx_gt_i32_e32 19, v70
	v_mov_b32_e32 v59, v248
	v_cmpx_gt_i32_e32 18, v70
	v_mov_b32_e32 v58, v248
	v_cmpx_gt_i32_e32 17, v70
	v_mov_b32_e32 v57, v248
	v_cmpx_gt_i32_e32 16, v70
	v_mov_b32_e32 v56, v248
	v_cmpx_gt_i32_e32 11, v70
	v_mov_b32_e32 v55, v248
	v_cmpx_gt_i32_e32 10, v70
	v_mov_b32_e32 v54, v248
	v_cmpx_gt_i32_e32 9, v70
	v_mov_b32_e32 v53, v248
	v_cmpx_gt_i32_e32 8, v70
	v_mov_b32_e32 v52, v248
	v_cmpx_gt_i32_e32 3, v70
	v_mov_b32_e32 v51, v248
	v_cmpx_gt_i32_e32 2, v70
	v_mov_b32_e32 v50, v248
	v_cmpx_gt_i32_e32 1, v70
	v_mov_b32_e32 v49, v248
	v_cmpx_gt_i32_e32 0, v70
	v_mov_b32_e32 v48, v248
.Lmaskx_done_9:
	s_mov_b64 exec, s[100:101]
	s_nop 4
	s_branch .LBB0_479
.Lmask_dead_9:
	v_mov_b32_e32 v32, 0
	v_mov_b32_e32 v49, 0
	v_mov_b32_e32 v48, 0
	v_mov_b32_e32 v33, 0
	v_mov_b32_e32 v50, 0
	v_mov_b32_e32 v34, 0
	v_mov_b32_e32 v51, 0
	v_mov_b32_e32 v35, 0
	v_mov_b32_e32 v52, 0
	v_mov_b32_e32 v36, 0
	v_mov_b32_e32 v53, 0
	v_mov_b32_e32 v37, 0
	v_mov_b32_e32 v54, 0
	v_mov_b32_e32 v38, 0
	v_mov_b32_e32 v55, 0
	v_mov_b32_e32 v39, 0
	v_mov_b32_e32 v56, 0
	v_mov_b32_e32 v40, 0
	v_mov_b32_e32 v57, 0
	v_mov_b32_e32 v41, 0
	v_mov_b32_e32 v58, 0
	v_mov_b32_e32 v42, 0
	v_mov_b32_e32 v59, 0
	v_mov_b32_e32 v43, 0
	v_mov_b32_e32 v60, 0
	v_mov_b32_e32 v44, 0
	v_mov_b32_e32 v61, 0
	v_mov_b32_e32 v45, 0
	v_mov_b32_e32 v62, 0
	v_mov_b32_e32 v46, 0
	v_mov_b32_e32 v63, 0
	v_mov_b32_e32 v47, 0
	v_add_f32_e32 v198, v235, v68
	s_mov_b64 s[0:1], 0
	v_lshl_add_u32 v68, s18, 8, v234
	s_ashr_i32 s18, s18, 2
	v_bfe_u32 v69, v231, s18, 1
	v_cmp_eq_u32_e32 vcc, 0, v69
	s_nop 1
	v_cndmask_b32_e32 v69, v68, v196, vcc
	v_cndmask_b32_e64 v76, v69, v68, s[40:41]
	s_waitcnt lgkmcnt(14)
	v_mfma_f32_32x32x16_f16 v[16:31], v[144:147], v[180:183], v[16:31]
	ds_read_b128 v[156:159], v76
	ds_read_b128 v[68:71], v76 offset:128
	s_waitcnt lgkmcnt(14)
	v_mfma_f32_32x32x16_f16 v[0:15], v[144:147], v[176:179], v[0:15]
	ds_read_b128 v[168:171], v76 offset:32
	ds_read_b128 v[200:203], v76 offset:160
	v_add_u32_e32 v144, s68, v232
	ds_read_b128 v[188:191], v144
	ds_read_b128 v[148:151], v144 offset:512
	s_waitcnt lgkmcnt(14)
	v_mfma_f32_32x32x16_f16 v[16:31], v[140:143], v[172:175], v[16:31]
	ds_read_b128 v[88:91], v76 offset:64
	ds_read_b128 v[72:75], v76 offset:192
	ds_read_b128 v[184:187], v144 offset:2048
	ds_read_b128 v[172:175], v144 offset:2560
	v_mfma_f32_32x32x16_f16 v[0:15], v[140:143], v[84:87], v[0:15]
	ds_read_b128 v[92:95], v76 offset:96
	ds_read_b128 v[76:79], v76 offset:224
	ds_read_b128 v[176:179], v144 offset:4096
	ds_read_b128 v[164:167], v144 offset:4608
	s_waitcnt lgkmcnt(14)
	v_mfma_f32_32x32x16_f16 v[16:31], v[136:139], v[80:83], v[16:31]
	s_waitcnt lgkmcnt(13)
	v_pk_add_f32 v[80:81], v[156:157], v[218:219] op_sel_hi:[1,0] neg_lo:[0,1] neg_hi:[0,1]
	v_pk_add_f32 v[82:83], v[158:159], v[218:219] op_sel_hi:[1,0] neg_lo:[0,1] neg_hi:[0,1]
	s_waitcnt lgkmcnt(11)
	v_pk_add_f32 v[84:85], v[168:169], v[218:219] op_sel_hi:[1,0] neg_lo:[0,1] neg_hi:[0,1]
	v_pk_add_f32 v[86:87], v[170:171], v[218:219] op_sel_hi:[1,0] neg_lo:[0,1] neg_hi:[0,1]
	s_waitcnt lgkmcnt(3)
	ds_read_b128 v[180:183], v144 offset:6144
	ds_read_b128 v[168:171], v144 offset:6656
	v_mfma_f32_32x32x16_f16 v[0:15], v[136:139], v[160:163], v[0:15]
	v_pk_add_f32 v[88:89], v[88:89], v[218:219] op_sel_hi:[1,0] neg_lo:[0,1] neg_hi:[0,1]
	v_pk_add_f32 v[90:91], v[90:91], v[218:219] op_sel_hi:[1,0] neg_lo:[0,1] neg_hi:[0,1]
	v_pk_add_f32 v[92:93], v[92:93], v[218:219] op_sel_hi:[1,0] neg_lo:[0,1] neg_hi:[0,1]
	v_pk_add_f32 v[94:95], v[94:95], v[218:219] op_sel_hi:[1,0] neg_lo:[0,1] neg_hi:[0,1]
	s_nop 0
	v_mfma_f32_32x32x16_f16 v[16:31], v[132:135], v[64:67], v[16:31]
	v_pk_add_f32 v[64:65], v[68:69], v[218:219] op_sel_hi:[1,0] neg_lo:[0,1] neg_hi:[0,1]
	v_pk_add_f32 v[66:67], v[70:71], v[218:219] op_sel_hi:[1,0] neg_lo:[0,1] neg_hi:[0,1]
	v_pk_add_f32 v[68:69], v[200:201], v[218:219] op_sel_hi:[1,0] neg_lo:[0,1] neg_hi:[0,1]
	v_pk_add_f32 v[70:71], v[202:203], v[218:219] op_sel_hi:[1,0] neg_lo:[0,1] neg_hi:[0,1]
	s_waitcnt lgkmcnt(4)
	v_mfma_f32_32x32x16_f16 v[0:15], v[132:135], v[152:155], v[0:15]
	v_pk_add_f32 v[72:73], v[72:73], v[218:219] op_sel_hi:[1,0] neg_lo:[0,1] neg_hi:[0,1]
	v_pk_add_f32 v[74:75], v[74:75], v[218:219] op_sel_hi:[1,0] neg_lo:[0,1] neg_hi:[0,1]
	v_pk_add_f32 v[76:77], v[76:77], v[218:219] op_sel_hi:[1,0] neg_lo:[0,1] neg_hi:[0,1]
	v_pk_add_f32 v[78:79], v[78:79], v[218:219] op_sel_hi:[1,0] neg_lo:[0,1] neg_hi:[0,1]
	s_nop 0
	s_waitcnt vmcnt(2) lgkmcnt(0)
	s_barrier
	s_andn2_b64 vcc, exec, s[0:1]
	s_branch .LBB0_482

; __device__ __forceinline__ void cmask(f32x16& p0, f32x16& p1, int jb, int qrel, int hi) {
;     const float NEG = -INFINITY; int kb = 64 * jb + 4 * hi;
; #pragma unroll
;     for (int r = 0; r < 16; ++r) { int kv = kb + (r & 3) + 8 * (r >> 2); if (kv > qrel) p0[r] = NEG; if (kv + 32 > qrel) p1[r] = NEG; }
; }
.LBB0_482:
	s_add_i32 s0, s68, 0x2000
	s_cmpk_lg_i32 s68, 0x4000
	s_cselect_b32 s45, s0, 0
	v_add_u32_e32 v160, s70, v230
	ds_read_b64_tr_b16 v[156:157], v160 offset:24576
	ds_read_b64_tr_b16 v[158:159], v160 offset:25088
	v_mfma_f32_32x32x16_f16 v[80:95], v[188:191], v[128:131], v[80:95]
	v_add_f32_e32 v132, v48, v49
	v_add_f32_e32 v132, v50, v132
	v_add_f32_e32 v132, v51, v132
	v_add_f32_e32 v132, v52, v132
	v_add_f32_e32 v132, v53, v132
	v_cvt_pk_f16_f32 v144, v48, v49
	v_cvt_pk_f16_f32 v145, v50, v51
	ds_read_b64_tr_b16 v[152:153], v160 offset:28672
	ds_read_b64_tr_b16 v[154:155], v160 offset:29184
	v_mfma_f32_32x32x16_f16 v[64:79], v[148:151], v[128:131], v[64:79]
	v_add_f32_e32 v48, v54, v132
	v_add_f32_e32 v48, v55, v48
	v_add_f32_e32 v48, v56, v48
	v_add_f32_e32 v48, v57, v48
	v_cvt_pk_f16_f32 v146, v52, v53
	v_cvt_pk_f16_f32 v147, v54, v55
	ds_read_b64_tr_b16 v[148:149], v160 offset:25600
	ds_read_b64_tr_b16 v[150:151], v160 offset:26112
	v_mfma_f32_32x32x16_f16 v[80:95], v[184:187], v[124:127], v[80:95]
	v_add_f32_e32 v48, v58, v48
	v_add_f32_e32 v48, v59, v48
	v_add_f32_e32 v48, v60, v48
	v_add_f32_e32 v48, v61, v48
	v_cvt_pk_f16_f32 v140, v56, v57
	v_cvt_pk_f16_f32 v141, v58, v59
	ds_read_b64_tr_b16 v[52:53], v160 offset:29696
	ds_read_b64_tr_b16 v[54:55], v160 offset:30208
	v_mfma_f32_32x32x16_f16 v[64:79], v[172:175], v[124:127], v[64:79]
	v_add_f32_e32 v48, v62, v48
	v_add_f32_e32 v48, v63, v48
	v_add_f32_e32 v48, v32, v48
	v_add_f32_e32 v56, v33, v48
	v_cvt_pk_f16_f32 v142, v60, v61
	v_cvt_pk_f16_f32 v143, v62, v63
	ds_read_b64_tr_b16 v[48:49], v160 offset:26624
	ds_read_b64_tr_b16 v[50:51], v160 offset:27136
	s_waitcnt lgkmcnt(13)
	v_mfma_f32_32x32x16_f16 v[80:95], v[176:179], v[120:123], v[80:95]
	v_add_f32_e32 v56, v34, v56
	v_add_f32_e32 v56, v35, v56
	v_add_f32_e32 v56, v36, v56
	v_add_f32_e32 v56, v37, v56
	v_cvt_pk_f16_f32 v136, v32, v33
	v_cvt_pk_f16_f32 v137, v34, v35
	ds_read_b64_tr_b16 v[184:185], v160 offset:30720
	ds_read_b64_tr_b16 v[186:187], v160 offset:31232
	s_waitcnt lgkmcnt(14)
	v_mfma_f32_32x32x16_f16 v[64:79], v[164:167], v[120:123], v[64:79]
	v_add_f32_e32 v32, v38, v56
	v_add_f32_e32 v32, v39, v32
	v_add_f32_e32 v32, v40, v32
	v_add_f32_e32 v56, v41, v32
	v_cvt_pk_f16_f32 v138, v36, v37
	v_cvt_pk_f16_f32 v139, v38, v39
	ds_read_b64_tr_b16 v[32:33], v160 offset:27648
	ds_read_b64_tr_b16 v[34:35], v160 offset:28160
	s_waitcnt lgkmcnt(14)
	v_mfma_f32_32x32x16_f16 v[80:95], v[180:183], v[116:119], v[80:95]
	v_add_f32_e32 v36, v42, v56
	v_add_f32_e32 v36, v43, v36
	v_add_f32_e32 v36, v44, v36
	v_add_f32_e32 v36, v45, v36
	v_cvt_pk_f16_f32 v132, v40, v41
	v_cvt_pk_f16_f32 v133, v42, v43
	ds_read_b64_tr_b16 v[180:181], v160 offset:31744
	ds_read_b64_tr_b16 v[182:183], v160 offset:32256
	v_mfma_f32_32x32x16_f16 v[64:79], v[168:171], v[116:119], v[64:79]
	v_add_f32_e32 v36, v46, v36
	v_add_f32_e32 v36, v47, v36
	v_add_f32_e32 v36, 0, v36
	v_cvt_pk_f16_f32 v134, v44, v45
	v_cvt_pk_f16_f32 v135, v46, v47
	s_add_i32 s0, s68, s89
	v_lshl_add_u64 v[38:39], v[194:195], 0, s[30:31]
	s_mov_b32 s1, m0
	s_mov_b32 m0, s0
	s_nop 0
	global_load_lds_dwordx4 v[38:39], off
	s_mov_b32 m0, s1
	s_cmp_lt_u32 s69, 2
	s_cselect_b64 s[0:1], -1, 0
	s_and_b64 s[18:19], s[0:1], exec
	s_cselect_b32 s18, s51, -2
	s_add_i32 s18, s18, s69
	v_mad_i64_i32 v[38:39], s[46:47], s18, v249, v[216:217]
	s_add_i32 s19, s45, s36
	s_mov_b32 s46, m0
	s_mov_b32 m0, s19
	s_nop 0
	global_load_lds_dwordx4 v[38:39], off
	s_mov_b32 m0, s46
	s_andn2_b64 vcc, exec, s[40:41]
	s_cbranch_vccnz .LBB0_484
	s_mov_b64 s[100:101], exec
	v_sub_u32_e32 v38, v215, v197
	v_add_u32_e32 v38, 59, v38
	v_cmp_gt_i32_e32 vcc, 0, v38
	s_cmp_eq_u64 vcc, exec
	s_cbranch_scc1 .Lmask_dead_8
	v_cmpx_gt_i32_e32 59, v38
	s_nop 3
	s_cbranch_execz .Lmaskx_done_8
	v_mov_b32_e32 v79, v248
	v_cmpx_gt_i32_e32 58, v38
	v_mov_b32_e32 v78, v248
	v_cmpx_gt_i32_e32 57, v38
	v_mov_b32_e32 v77, v248
	v_cmpx_gt_i32_e32 56, v38
	v_mov_b32_e32 v76, v248
	v_cmpx_gt_i32_e32 51, v38
	v_mov_b32_e32 v75, v248
	v_cmpx_gt_i32_e32 50, v38
	v_mov_b32_e32 v74, v248
	v_cmpx_gt_i32_e32 49, v38
	v_mov_b32_e32 v73, v248
	v_cmpx_gt_i32_e32 48, v38
	v_mov_b32_e32 v72, v248
	v_cmpx_gt_i32_e32 43, v38
	v_mov_b32_e32 v71, v248
	v_cmpx_gt_i32_e32 42, v38
	v_mov_b32_e32 v70, v248
	v_cmpx_gt_i32_e32 41, v38
	v_mov_b32_e32 v69, v248
	v_cmpx_gt_i32_e32 40, v38
	v_mov_b32_e32 v68, v248
	v_cmpx_gt_i32_e32 35, v38
	v_mov_b32_e32 v67, v248
	v_cmpx_gt_i32_e32 34, v38
	v_mov_b32_e32 v66, v248
	v_cmpx_gt_i32_e32 33, v38
	v_mov_b32_e32 v65, v248
	v_cmpx_gt_i32_e32 32, v38
	v_mov_b32_e32 v64, v248
	v_cmpx_gt_i32_e32 27, v38
	v_mov_b32_e32 v95, v248
	v_cmpx_gt_i32_e32 26, v38
	v_mov_b32_e32 v94, v248
	v_cmpx_gt_i32_e32 25, v38
	v_mov_b32_e32 v93, v248
	v_cmpx_gt_i32_e32 24, v38
	v_mov_b32_e32 v92, v248
	v_cmpx_gt_i32_e32 19, v38
	v_mov_b32_e32 v91, v248
	v_cmpx_gt_i32_e32 18, v38
	v_mov_b32_e32 v90, v248
	v_cmpx_gt_i32_e32 17, v38
	v_mov_b32_e32 v89, v248
	v_cmpx_gt_i32_e32 16, v38
	v_mov_b32_e32 v88, v248
	v_cmpx_gt_i32_e32 11, v38
	v_mov_b32_e32 v87, v248
	v_cmpx_gt_i32_e32 10, v38
	v_mov_b32_e32 v86, v248
	v_cmpx_gt_i32_e32 9, v38
	v_mov_b32_e32 v85, v248
	v_cmpx_gt_i32_e32 8, v38
	v_mov_b32_e32 v84, v248
	v_cmpx_gt_i32_e32 3, v38
	v_mov_b32_e32 v83, v248
	v_cmpx_gt_i32_e32 2, v38
	v_mov_b32_e32 v82, v248
	v_cmpx_gt_i32_e32 1, v38
	v_mov_b32_e32 v81, v248
	v_cmpx_gt_i32_e32 0, v38
	v_mov_b32_e32 v80, v248

; #define WAIT_BAR(N) asm volatile("s_waitcnt vmcnt(" #N ") lgkmcnt(0)\n\ts_barrier" ::: "memory")
; #define RESC() do { if (resc) { asm volatile("s_waitcnt lgkmcnt(0)" ::: "memory"); \
;       _Pragma("unroll") for (int d_ = 0; d_ < 2; ++d_) _Pragma("unroll") for (int r = 0; r < 16; ++r) o[d_][r] *= wsf[crow(r, hi)]; } } while (0)
; #define ROT() do { sl_prev = sl_cur; sl_cur = sl_next; sl_next = (sl_next == (NSLOT - 1) * SLOTB) ? 0 : sl_next + SLOTB; } while (0)
; template <bool MOBA, int THRL> ...
;     ...
;     int t = 1;
;     ...
;     for (; t + 5 < NT; t += 2) {
;         STEP(pB0, pB1, pA0, pA1, t, true, true, true);       WAIT_BAR(2); RESC(); ROT();
.Lmask_dead_8:
	v_mov_b32_e32 v64, 0
	v_mov_b32_e32 v81, 0
	v_mov_b32_e32 v80, 0
	v_mov_b32_e32 v65, 0
	v_mov_b32_e32 v82, 0
	v_mov_b32_e32 v66, 0
	v_mov_b32_e32 v83, 0
	v_mov_b32_e32 v67, 0
	v_mov_b32_e32 v84, 0
	v_mov_b32_e32 v68, 0
	v_mov_b32_e32 v85, 0
	v_mov_b32_e32 v69, 0
	v_mov_b32_e32 v86, 0
	v_mov_b32_e32 v70, 0
	v_mov_b32_e32 v87, 0
	v_mov_b32_e32 v71, 0
	v_mov_b32_e32 v88, 0
	v_mov_b32_e32 v72, 0
	v_mov_b32_e32 v89, 0
	v_mov_b32_e32 v73, 0
	v_mov_b32_e32 v90, 0
	v_mov_b32_e32 v74, 0
	v_mov_b32_e32 v91, 0
	v_mov_b32_e32 v75, 0
	v_mov_b32_e32 v92, 0
	v_mov_b32_e32 v76, 0
	v_mov_b32_e32 v93, 0
	v_mov_b32_e32 v77, 0
	v_mov_b32_e32 v94, 0
	v_mov_b32_e32 v78, 0
	v_mov_b32_e32 v95, 0
	v_mov_b32_e32 v79, 0
	v_add_f32_e32 v235, v198, v36
	s_mov_b64 s[40:41], 0
	v_lshl_add_u32 v36, s18, 8, v234
	s_ashr_i32 s18, s18, 2
	v_bfe_u32 v37, v231, s18, 1
	v_cmp_eq_u32_e32 vcc, 0, v37
	s_nop 1
	v_cndmask_b32_e32 v37, v36, v196, vcc
	v_cndmask_b32_e64 v44, v37, v36, s[0:1]
	s_waitcnt lgkmcnt(14)
	v_mfma_f32_32x32x16_f16 v[16:31], v[144:147], v[156:159], v[16:31]
	ds_read_b128 v[156:159], v44
	ds_read_b128 v[36:39], v44 offset:128
	s_waitcnt lgkmcnt(14)
	v_mfma_f32_32x32x16_f16 v[0:15], v[144:147], v[152:155], v[0:15]
	ds_read_b128 v[188:191], v44 offset:32
	ds_read_b128 v[198:201], v44 offset:160
	v_add_u32_e32 v144, s45, v232
	ds_read_b128 v[176:179], v144
	ds_read_b128 v[172:175], v144 offset:512
	s_waitcnt lgkmcnt(14)
	v_mfma_f32_32x32x16_f16 v[16:31], v[140:143], v[148:151], v[16:31]
	ds_read_b128 v[56:59], v44 offset:64
	ds_read_b128 v[40:43], v44 offset:192
	ds_read_b128 v[168:171], v144 offset:2048
	ds_read_b128 v[164:167], v144 offset:2560
	v_mfma_f32_32x32x16_f16 v[0:15], v[140:143], v[52:55], v[0:15]
	ds_read_b128 v[60:63], v44 offset:96
	ds_read_b128 v[44:47], v44 offset:224
	ds_read_b128 v[160:163], v144 offset:4096
	ds_read_b128 v[152:155], v144 offset:4608
	s_waitcnt lgkmcnt(14)
	v_mfma_f32_32x32x16_f16 v[16:31], v[136:139], v[48:51], v[16:31]
	s_waitcnt lgkmcnt(13)
	v_pk_add_f32 v[48:49], v[156:157], v[218:219] op_sel_hi:[1,0] neg_lo:[0,1] neg_hi:[0,1]
	v_pk_add_f32 v[50:51], v[158:159], v[218:219] op_sel_hi:[1,0] neg_lo:[0,1] neg_hi:[0,1]
	s_waitcnt lgkmcnt(11)
	v_pk_add_f32 v[52:53], v[188:189], v[218:219] op_sel_hi:[1,0] neg_lo:[0,1] neg_hi:[0,1]
	v_pk_add_f32 v[54:55], v[190:191], v[218:219] op_sel_hi:[1,0] neg_lo:[0,1] neg_hi:[0,1]
	s_waitcnt lgkmcnt(3)
	ds_read_b128 v[156:159], v144 offset:6144
	ds_read_b128 v[148:151], v144 offset:6656
	v_mfma_f32_32x32x16_f16 v[0:15], v[136:139], v[184:187], v[0:15]
	v_pk_add_f32 v[56:57], v[56:57], v[218:219] op_sel_hi:[1,0] neg_lo:[0,1] neg_hi:[0,1]
	v_pk_add_f32 v[58:59], v[58:59], v[218:219] op_sel_hi:[1,0] neg_lo:[0,1] neg_hi:[0,1]
	v_pk_add_f32 v[60:61], v[60:61], v[218:219] op_sel_hi:[1,0] neg_lo:[0,1] neg_hi:[0,1]
	v_pk_add_f32 v[62:63], v[62:63], v[218:219] op_sel_hi:[1,0] neg_lo:[0,1] neg_hi:[0,1]
	s_nop 0
	v_mfma_f32_32x32x16_f16 v[16:31], v[132:135], v[32:35], v[16:31]
	v_pk_add_f32 v[32:33], v[36:37], v[218:219] op_sel_hi:[1,0] neg_lo:[0,1] neg_hi:[0,1]
	v_pk_add_f32 v[34:35], v[38:39], v[218:219] op_sel_hi:[1,0] neg_lo:[0,1] neg_hi:[0,1]
	v_pk_add_f32 v[36:37], v[198:199], v[218:219] op_sel_hi:[1,0] neg_lo:[0,1] neg_hi:[0,1]
	v_pk_add_f32 v[38:39], v[200:201], v[218:219] op_sel_hi:[1,0] neg_lo:[0,1] neg_hi:[0,1]
	s_waitcnt lgkmcnt(4)
	v_mfma_f32_32x32x16_f16 v[0:15], v[132:135], v[180:183], v[0:15]
	v_pk_add_f32 v[40:41], v[40:41], v[218:219] op_sel_hi:[1,0] neg_lo:[0,1] neg_hi:[0,1]
	v_pk_add_f32 v[42:43], v[42:43], v[218:219] op_sel_hi:[1,0] neg_lo:[0,1] neg_hi:[0,1]
	v_pk_add_f32 v[44:45], v[44:45], v[218:219] op_sel_hi:[1,0] neg_lo:[0,1] neg_hi:[0,1]
	v_pk_add_f32 v[46:47], v[46:47], v[218:219] op_sel_hi:[1,0] neg_lo:[0,1] neg_hi:[0,1]
	s_nop 0
	s_waitcnt vmcnt(2) lgkmcnt(0)
	s_barrier
	s_andn2_b64 vcc, exec, s[40:41]
	s_branch .LBB0_487

; __device__ __forceinline__ void cmask(f32x16& p0, f32x16& p1, int jb, int qrel, int hi) {
;     const float NEG = -INFINITY; int kb = 64 * jb + 4 * hi;
; #pragma unroll
;     for (int r = 0; r < 16; ++r) { int kv = kb + (r & 3) + 8 * (r >> 2); if (kv > qrel) p0[r] = NEG; if (kv + 32 > qrel) p1[r] = NEG; }
; }
.LBB0_625:
	v_add_u32_e32 v184, s40, v229
	ds_read_b64_tr_b16 v[180:181], v184 offset:24576
	ds_read_b64_tr_b16 v[182:183], v184 offset:25088
	s_waitcnt lgkmcnt(9)
	v_mfma_f32_32x32x16_f16 v[48:63], v[176:179], v[128:131], v[48:63]
	v_add_f32_e32 v132, v80, v81
	v_add_f32_e32 v132, v82, v132
	v_add_f32_e32 v132, v83, v132
	v_add_f32_e32 v132, v84, v132
	v_add_f32_e32 v132, v85, v132
	v_cvt_pk_f16_f32 v144, v80, v81
	v_cvt_pk_f16_f32 v145, v82, v83
	ds_read_b64_tr_b16 v[176:177], v184 offset:28672
	ds_read_b64_tr_b16 v[178:179], v184 offset:29184
	s_waitcnt lgkmcnt(10)
	v_mfma_f32_32x32x16_f16 v[32:47], v[172:175], v[128:131], v[32:47]
	v_add_f32_e32 v80, v86, v132
	v_add_f32_e32 v80, v87, v80
	v_add_f32_e32 v80, v88, v80
	v_add_f32_e32 v80, v89, v80
	v_cvt_pk_f16_f32 v146, v84, v85
	v_cvt_pk_f16_f32 v147, v86, v87
	ds_read_b64_tr_b16 v[172:173], v184 offset:25600
	ds_read_b64_tr_b16 v[174:175], v184 offset:26112
	s_waitcnt lgkmcnt(11)
	v_mfma_f32_32x32x16_f16 v[48:63], v[168:171], v[124:127], v[48:63]
	v_add_f32_e32 v80, v90, v80
	v_add_f32_e32 v80, v91, v80
	v_add_f32_e32 v80, v92, v80
	v_add_f32_e32 v80, v93, v80
	v_cvt_pk_f16_f32 v140, v88, v89
	v_cvt_pk_f16_f32 v141, v90, v91
	ds_read_b64_tr_b16 v[84:85], v184 offset:29696
	ds_read_b64_tr_b16 v[86:87], v184 offset:30208
	s_waitcnt lgkmcnt(12)
	v_mfma_f32_32x32x16_f16 v[32:47], v[164:167], v[124:127], v[32:47]
	v_add_f32_e32 v80, v94, v80
	v_add_f32_e32 v80, v95, v80
	v_add_f32_e32 v80, v64, v80
	v_add_f32_e32 v88, v65, v80
	v_cvt_pk_f16_f32 v142, v92, v93
	v_cvt_pk_f16_f32 v143, v94, v95
	ds_read_b64_tr_b16 v[80:81], v184 offset:26624
	ds_read_b64_tr_b16 v[82:83], v184 offset:27136
	s_waitcnt lgkmcnt(13)
	v_mfma_f32_32x32x16_f16 v[48:63], v[160:163], v[120:123], v[48:63]
	v_add_f32_e32 v88, v66, v88
	v_add_f32_e32 v88, v67, v88
	v_add_f32_e32 v88, v68, v88
	v_add_f32_e32 v88, v69, v88
	v_cvt_pk_f16_f32 v136, v64, v65
	v_cvt_pk_f16_f32 v137, v66, v67
	ds_read_b64_tr_b16 v[160:161], v184 offset:30720
	ds_read_b64_tr_b16 v[162:163], v184 offset:31232
	s_waitcnt lgkmcnt(14)
	v_mfma_f32_32x32x16_f16 v[32:47], v[152:155], v[120:123], v[32:47]
	v_add_f32_e32 v64, v70, v88
	v_add_f32_e32 v64, v71, v64
	v_add_f32_e32 v64, v72, v64
	v_add_f32_e32 v88, v73, v64
	v_cvt_pk_f16_f32 v138, v68, v69
	v_cvt_pk_f16_f32 v139, v70, v71
	ds_read_b64_tr_b16 v[64:65], v184 offset:27648
	ds_read_b64_tr_b16 v[66:67], v184 offset:28160
	s_waitcnt lgkmcnt(14)
	v_mfma_f32_32x32x16_f16 v[48:63], v[156:159], v[116:119], v[48:63]
	v_add_f32_e32 v68, v74, v88
	v_add_f32_e32 v68, v75, v68
	v_add_f32_e32 v68, v76, v68
	v_add_f32_e32 v68, v77, v68
	v_cvt_pk_f16_f32 v132, v72, v73
	v_cvt_pk_f16_f32 v133, v74, v75
	ds_read_b64_tr_b16 v[152:153], v184 offset:31744
	ds_read_b64_tr_b16 v[154:155], v184 offset:32256
	v_mfma_f32_32x32x16_f16 v[32:47], v[148:151], v[116:119], v[32:47]
	v_add_f32_e32 v68, v78, v68
	v_add_f32_e32 v68, v79, v68
	v_add_f32_e32 v68, 0, v68
	v_cvt_pk_f16_f32 v134, v76, v77
	v_cvt_pk_f16_f32 v135, v78, v79
	v_lshl_add_u64 v[70:71], v[194:195], 0, s[30:31]
	s_add_i32 s11, s69, s90
	s_mov_b32 s18, m0
	s_mov_b32 m0, s11
	s_nop 0
	global_load_lds_dwordx4 v[70:71], off
	s_mov_b32 m0, s18
	s_add_i32 s18, s26, s45
	s_add_i32 s37, s26, s19
	s_add_i32 s11, s18, 1
	s_add_i32 s66, s37, 1
	s_cmp_lt_u32 s45, 3
	s_cselect_b64 s[40:41], -1, 0
	s_and_b64 s[50:51], s[40:41], exec
	s_cselect_b32 s11, s11, s66
	v_mad_i64_i32 v[70:71], s[50:51], s11, v249, v[216:217]
	s_add_i32 s50, s68, s10
	s_mov_b32 s51, m0
	s_mov_b32 m0, s50
	s_nop 0
	global_load_lds_dwordx4 v[70:71], off
	s_mov_b32 m0, s51
	s_cmp_gt_u32 s45, 3
	s_cbranch_scc1 .LBB0_627
	s_mov_b64 s[100:101], exec
	v_sub_u32_e32 v69, v215, v196
	v_add_u32_e32 v69, 32, v69
	v_cmp_gt_i32_e32 vcc, 0, v69
	s_cmp_eq_u64 vcc, exec
	s_cbranch_scc1 .Lmask_dead_4
	v_cmpx_gt_i32_e32 59, v69
	s_nop 3
	s_cbranch_execz .Lmaskx_done_4
	v_mov_b32_e32 v47, v248
	v_cmpx_gt_i32_e32 58, v69
	v_mov_b32_e32 v46, v248
	v_cmpx_gt_i32_e32 57, v69
	v_mov_b32_e32 v45, v248
	v_cmpx_gt_i32_e32 56, v69
	v_mov_b32_e32 v44, v248
	v_cmpx_gt_i32_e32 51, v69
	v_mov_b32_e32 v43, v248
	v_cmpx_gt_i32_e32 50, v69
	v_mov_b32_e32 v42, v248
	v_cmpx_gt_i32_e32 49, v69
	v_mov_b32_e32 v41, v248
	v_cmpx_gt_i32_e32 48, v69
	v_mov_b32_e32 v40, v248
	v_cmpx_gt_i32_e32 43, v69
	v_mov_b32_e32 v39, v248
	v_cmpx_gt_i32_e32 42, v69
	v_mov_b32_e32 v38, v248
	v_cmpx_gt_i32_e32 41, v69
	v_mov_b32_e32 v37, v248
	v_cmpx_gt_i32_e32 40, v69
	v_mov_b32_e32 v36, v248
	v_cmpx_gt_i32_e32 35, v69
	v_mov_b32_e32 v35, v248
	v_cmpx_gt_i32_e32 34, v69
	v_mov_b32_e32 v34, v248
	v_cmpx_gt_i32_e32 33, v69
	v_mov_b32_e32 v33, v248
	v_cmpx_gt_i32_e32 32, v69
	v_mov_b32_e32 v32, v248
	v_cmpx_gt_i32_e32 27, v69
	v_mov_b32_e32 v63, v248
	v_cmpx_gt_i32_e32 26, v69
	v_mov_b32_e32 v62, v248
	v_cmpx_gt_i32_e32 25, v69
	v_mov_b32_e32 v61, v248
	v_cmpx_gt_i32_e32 24, v69
	v_mov_b32_e32 v60, v248
	v_cmpx_gt_i32_e32 19, v69
	v_mov_b32_e32 v59, v248
	v_cmpx_gt_i32_e32 18, v69
	v_mov_b32_e32 v58, v248
	v_cmpx_gt_i32_e32 17, v69
	v_mov_b32_e32 v57, v248
	v_cmpx_gt_i32_e32 16, v69
	v_mov_b32_e32 v56, v248
	v_cmpx_gt_i32_e32 11, v69
	v_mov_b32_e32 v55, v248
	v_cmpx_gt_i32_e32 10, v69
	v_mov_b32_e32 v54, v248
	v_cmpx_gt_i32_e32 9, v69
	v_mov_b32_e32 v53, v248
	v_cmpx_gt_i32_e32 8, v69
	v_mov_b32_e32 v52, v248
	v_cmpx_gt_i32_e32 3, v69
	v_mov_b32_e32 v51, v248
	v_cmpx_gt_i32_e32 2, v69
	v_mov_b32_e32 v50, v248
	v_cmpx_gt_i32_e32 1, v69
	v_mov_b32_e32 v49, v248
	v_cmpx_gt_i32_e32 0, v69
	v_mov_b32_e32 v48, v248

.Lmask_dead_4:
	v_mov_b32_e32 v32, 0
	v_mov_b32_e32 v49, 0
	v_mov_b32_e32 v48, 0
	v_mov_b32_e32 v33, 0
	v_mov_b32_e32 v50, 0
	v_mov_b32_e32 v34, 0
	v_mov_b32_e32 v51, 0
	v_mov_b32_e32 v35, 0
	v_mov_b32_e32 v52, 0
	v_mov_b32_e32 v36, 0
	v_mov_b32_e32 v53, 0
	v_mov_b32_e32 v37, 0
	v_mov_b32_e32 v54, 0
	v_mov_b32_e32 v38, 0
	v_mov_b32_e32 v55, 0
	v_mov_b32_e32 v39, 0
	v_mov_b32_e32 v56, 0
	v_mov_b32_e32 v40, 0
	v_mov_b32_e32 v57, 0
	v_mov_b32_e32 v41, 0
	v_mov_b32_e32 v58, 0
	v_mov_b32_e32 v42, 0
	v_mov_b32_e32 v59, 0
	v_mov_b32_e32 v43, 0
	v_mov_b32_e32 v60, 0
	v_mov_b32_e32 v44, 0
	v_mov_b32_e32 v61, 0
	v_mov_b32_e32 v45, 0
	v_mov_b32_e32 v62, 0
	v_mov_b32_e32 v46, 0
	v_mov_b32_e32 v63, 0
	v_mov_b32_e32 v47, 0
	v_add_f32_e32 v197, v233, v68
	s_mov_b64 s[50:51], 0
	s_waitcnt lgkmcnt(14)
	v_mfma_f32_32x32x16_f16 v[16:31], v[144:147], v[180:183], v[16:31]
	v_lshl_add_u32 v76, s11, 8, v232
	ds_read_b128 v[156:159], v76
	ds_read_b128 v[68:71], v76 offset:128
	s_waitcnt lgkmcnt(14)
	v_mfma_f32_32x32x16_f16 v[0:15], v[144:147], v[176:179], v[0:15]
	ds_read_b128 v[168:171], v76 offset:32
	ds_read_b128 v[198:201], v76 offset:160
	v_add_u32_e32 v144, s68, v230
	ds_read_b128 v[188:191], v144
	ds_read_b128 v[148:151], v144 offset:512
	s_waitcnt lgkmcnt(14)
	v_mfma_f32_32x32x16_f16 v[16:31], v[140:143], v[172:175], v[16:31]
	ds_read_b128 v[88:91], v76 offset:64
	ds_read_b128 v[72:75], v76 offset:192
	ds_read_b128 v[184:187], v144 offset:2048
	ds_read_b128 v[172:175], v144 offset:2560
	v_mfma_f32_32x32x16_f16 v[0:15], v[140:143], v[84:87], v[0:15]
	ds_read_b128 v[92:95], v76 offset:96
	ds_read_b128 v[76:79], v76 offset:224
	ds_read_b128 v[176:179], v144 offset:4096
	ds_read_b128 v[164:167], v144 offset:4608
	s_waitcnt lgkmcnt(14)
	v_mfma_f32_32x32x16_f16 v[16:31], v[136:139], v[80:83], v[16:31]
	s_waitcnt lgkmcnt(13)
	v_pk_add_f32 v[80:81], v[156:157], v[218:219] op_sel_hi:[1,0] neg_lo:[0,1] neg_hi:[0,1]
	v_pk_add_f32 v[82:83], v[158:159], v[218:219] op_sel_hi:[1,0] neg_lo:[0,1] neg_hi:[0,1]
	s_waitcnt lgkmcnt(11)
	v_pk_add_f32 v[84:85], v[168:169], v[218:219] op_sel_hi:[1,0] neg_lo:[0,1] neg_hi:[0,1]
	v_pk_add_f32 v[86:87], v[170:171], v[218:219] op_sel_hi:[1,0] neg_lo:[0,1] neg_hi:[0,1]
	s_waitcnt lgkmcnt(3)
	ds_read_b128 v[180:183], v144 offset:6144
	ds_read_b128 v[168:171], v144 offset:6656
	v_mfma_f32_32x32x16_f16 v[0:15], v[136:139], v[160:163], v[0:15]
	v_pk_add_f32 v[88:89], v[88:89], v[218:219] op_sel_hi:[1,0] neg_lo:[0,1] neg_hi:[0,1]
	v_pk_add_f32 v[90:91], v[90:91], v[218:219] op_sel_hi:[1,0] neg_lo:[0,1] neg_hi:[0,1]
	v_pk_add_f32 v[92:93], v[92:93], v[218:219] op_sel_hi:[1,0] neg_lo:[0,1] neg_hi:[0,1]
	v_pk_add_f32 v[94:95], v[94:95], v[218:219] op_sel_hi:[1,0] neg_lo:[0,1] neg_hi:[0,1]
	s_nop 0
	v_mfma_f32_32x32x16_f16 v[16:31], v[132:135], v[64:67], v[16:31]
	v_pk_add_f32 v[64:65], v[68:69], v[218:219] op_sel_hi:[1,0] neg_lo:[0,1] neg_hi:[0,1]
	v_pk_add_f32 v[66:67], v[70:71], v[218:219] op_sel_hi:[1,0] neg_lo:[0,1] neg_hi:[0,1]
	v_pk_add_f32 v[68:69], v[198:199], v[218:219] op_sel_hi:[1,0] neg_lo:[0,1] neg_hi:[0,1]
	v_pk_add_f32 v[70:71], v[200:201], v[218:219] op_sel_hi:[1,0] neg_lo:[0,1] neg_hi:[0,1]
	s_waitcnt lgkmcnt(4)
	v_mfma_f32_32x32x16_f16 v[0:15], v[132:135], v[152:155], v[0:15]
	v_pk_add_f32 v[72:73], v[72:73], v[218:219] op_sel_hi:[1,0] neg_lo:[0,1] neg_hi:[0,1]
	v_pk_add_f32 v[74:75], v[74:75], v[218:219] op_sel_hi:[1,0] neg_lo:[0,1] neg_hi:[0,1]
	v_pk_add_f32 v[76:77], v[76:77], v[218:219] op_sel_hi:[1,0] neg_lo:[0,1] neg_hi:[0,1]
	v_pk_add_f32 v[78:79], v[78:79], v[218:219] op_sel_hi:[1,0] neg_lo:[0,1] neg_hi:[0,1]
	s_nop 0
	s_waitcnt vmcnt(2) lgkmcnt(0)
	s_barrier
	s_andn2_b64 vcc, exec, s[50:51]
	s_branch .LBB0_630

; __device__ __forceinline__ void cmask(f32x16& p0, f32x16& p1, int jb, int qrel, int hi) {
;     const float NEG = -INFINITY; int kb = 64 * jb + 4 * hi;
; #pragma unroll
;     for (int r = 0; r < 16; ++r) { int kv = kb + (r & 3) + 8 * (r >> 2); if (kv > qrel) p0[r] = NEG; if (kv + 32 > qrel) p1[r] = NEG; }
; }
.LBB0_630:
	s_add_i32 s11, s68, 0x2000
	s_cmpk_lg_i32 s68, 0x4000
	s_cselect_b32 s11, s11, 0
	v_add_u32_e32 v160, s69, v229
	ds_read_b64_tr_b16 v[156:157], v160 offset:24576
	ds_read_b64_tr_b16 v[158:159], v160 offset:25088
	v_mfma_f32_32x32x16_f16 v[80:95], v[188:191], v[128:131], v[80:95]
	v_add_f32_e32 v132, v48, v49
	v_add_f32_e32 v132, v50, v132
	v_add_f32_e32 v132, v51, v132
	v_add_f32_e32 v132, v52, v132
	v_add_f32_e32 v132, v53, v132
	v_cvt_pk_f16_f32 v144, v48, v49
	v_cvt_pk_f16_f32 v145, v50, v51
	ds_read_b64_tr_b16 v[152:153], v160 offset:28672
	ds_read_b64_tr_b16 v[154:155], v160 offset:29184
	v_mfma_f32_32x32x16_f16 v[64:79], v[148:151], v[128:131], v[64:79]
	v_add_f32_e32 v48, v54, v132
	v_add_f32_e32 v48, v55, v48
	v_add_f32_e32 v48, v56, v48
	v_add_f32_e32 v48, v57, v48
	v_cvt_pk_f16_f32 v146, v52, v53
	v_cvt_pk_f16_f32 v147, v54, v55
	ds_read_b64_tr_b16 v[148:149], v160 offset:25600
	ds_read_b64_tr_b16 v[150:151], v160 offset:26112
	v_mfma_f32_32x32x16_f16 v[80:95], v[184:187], v[124:127], v[80:95]
	v_add_f32_e32 v48, v58, v48
	v_add_f32_e32 v48, v59, v48
	v_add_f32_e32 v48, v60, v48
	v_add_f32_e32 v48, v61, v48
	v_cvt_pk_f16_f32 v140, v56, v57
	v_cvt_pk_f16_f32 v141, v58, v59
	ds_read_b64_tr_b16 v[52:53], v160 offset:29696
	ds_read_b64_tr_b16 v[54:55], v160 offset:30208
	v_mfma_f32_32x32x16_f16 v[64:79], v[172:175], v[124:127], v[64:79]
	v_add_f32_e32 v48, v62, v48
	v_add_f32_e32 v48, v63, v48
	v_add_f32_e32 v48, v32, v48
	v_add_f32_e32 v56, v33, v48
	v_cvt_pk_f16_f32 v142, v60, v61
	v_cvt_pk_f16_f32 v143, v62, v63
	ds_read_b64_tr_b16 v[48:49], v160 offset:26624
	ds_read_b64_tr_b16 v[50:51], v160 offset:27136
	s_waitcnt lgkmcnt(13)
	v_mfma_f32_32x32x16_f16 v[80:95], v[176:179], v[120:123], v[80:95]
	v_add_f32_e32 v56, v34, v56
	v_add_f32_e32 v56, v35, v56
	v_add_f32_e32 v56, v36, v56
	v_add_f32_e32 v56, v37, v56
	v_cvt_pk_f16_f32 v136, v32, v33
	v_cvt_pk_f16_f32 v137, v34, v35
	ds_read_b64_tr_b16 v[184:185], v160 offset:30720
	ds_read_b64_tr_b16 v[186:187], v160 offset:31232
	s_waitcnt lgkmcnt(14)
	v_mfma_f32_32x32x16_f16 v[64:79], v[164:167], v[120:123], v[64:79]
	v_add_f32_e32 v32, v38, v56
	v_add_f32_e32 v32, v39, v32
	v_add_f32_e32 v32, v40, v32
	v_add_f32_e32 v56, v41, v32
	v_cvt_pk_f16_f32 v138, v36, v37
	v_cvt_pk_f16_f32 v139, v38, v39
	ds_read_b64_tr_b16 v[32:33], v160 offset:27648
	ds_read_b64_tr_b16 v[34:35], v160 offset:28160
	s_waitcnt lgkmcnt(14)
	v_mfma_f32_32x32x16_f16 v[80:95], v[180:183], v[116:119], v[80:95]
	v_add_f32_e32 v36, v42, v56
	v_add_f32_e32 v36, v43, v36
	v_add_f32_e32 v36, v44, v36
	v_add_f32_e32 v36, v45, v36
	v_cvt_pk_f16_f32 v132, v40, v41
	v_cvt_pk_f16_f32 v133, v42, v43
	ds_read_b64_tr_b16 v[180:181], v160 offset:31744
	ds_read_b64_tr_b16 v[182:183], v160 offset:32256
	v_mfma_f32_32x32x16_f16 v[64:79], v[168:171], v[116:119], v[64:79]
	v_add_f32_e32 v36, v46, v36
	v_add_f32_e32 v36, v47, v36
	v_add_f32_e32 v36, 0, v36
	v_cvt_pk_f16_f32 v134, v44, v45
	v_cvt_pk_f16_f32 v135, v46, v47
	s_add_i32 s50, s68, s90
	s_add_i32 s18, s18, 2
	s_cmp_lt_u32 s45, 2
	s_mov_b32 s51, m0
	s_mov_b32 m0, s50
	s_nop 0
	global_load_lds_dwordx4 v[194:195], off
	s_mov_b32 m0, s51
	s_cselect_b32 s18, s18, s37
	v_mad_i64_i32 v[38:39], s[50:51], s18, v249, v[216:217]
	s_add_i32 s37, s11, s10
	s_mov_b32 s50, m0
	s_mov_b32 m0, s37
	s_nop 0
	global_load_lds_dwordx4 v[38:39], off
	s_mov_b32 m0, s50
	s_andn2_b64 vcc, exec, s[40:41]
	s_cbranch_vccnz .LBB0_632
	s_mov_b64 s[100:101], exec
	v_sub_u32_e32 v38, v215, v196
	v_add_u32_e32 v38, 0xffffffe0, v38
	v_cmp_gt_i32_e32 vcc, 0, v38
	s_cmp_eq_u64 vcc, exec
	s_cbranch_scc1 .Lmask_dead_3
	v_cmpx_gt_i32_e32 59, v38
	s_nop 3
	s_cbranch_execz .Lmaskx_done_3
	v_mov_b32_e32 v79, v248
	v_cmpx_gt_i32_e32 58, v38
	v_mov_b32_e32 v78, v248
	v_cmpx_gt_i32_e32 57, v38
	v_mov_b32_e32 v77, v248
	v_cmpx_gt_i32_e32 56, v38
	v_mov_b32_e32 v76, v248
	v_cmpx_gt_i32_e32 51, v38
	v_mov_b32_e32 v75, v248
	v_cmpx_gt_i32_e32 50, v38
	v_mov_b32_e32 v74, v248
	v_cmpx_gt_i32_e32 49, v38
	v_mov_b32_e32 v73, v248
	v_cmpx_gt_i32_e32 48, v38
	v_mov_b32_e32 v72, v248
	v_cmpx_gt_i32_e32 43, v38
	v_mov_b32_e32 v71, v248
	v_cmpx_gt_i32_e32 42, v38
	v_mov_b32_e32 v70, v248
	v_cmpx_gt_i32_e32 41, v38
	v_mov_b32_e32 v69, v248
	v_cmpx_gt_i32_e32 40, v38
	v_mov_b32_e32 v68, v248
	v_cmpx_gt_i32_e32 35, v38
	v_mov_b32_e32 v67, v248
	v_cmpx_gt_i32_e32 34, v38
	v_mov_b32_e32 v66, v248
	v_cmpx_gt_i32_e32 33, v38
	v_mov_b32_e32 v65, v248
	v_cmpx_gt_i32_e32 32, v38
	v_mov_b32_e32 v64, v248
	v_cmpx_gt_i32_e32 27, v38
	v_mov_b32_e32 v95, v248
	v_cmpx_gt_i32_e32 26, v38
	v_mov_b32_e32 v94, v248
	v_cmpx_gt_i32_e32 25, v38
	v_mov_b32_e32 v93, v248
	v_cmpx_gt_i32_e32 24, v38
	v_mov_b32_e32 v92, v248
	v_cmpx_gt_i32_e32 19, v38
	v_mov_b32_e32 v91, v248
	v_cmpx_gt_i32_e32 18, v38
	v_mov_b32_e32 v90, v248
	v_cmpx_gt_i32_e32 17, v38
	v_mov_b32_e32 v89, v248
	v_cmpx_gt_i32_e32 16, v38
	v_mov_b32_e32 v88, v248
	v_cmpx_gt_i32_e32 11, v38
	v_mov_b32_e32 v87, v248
	v_cmpx_gt_i32_e32 10, v38
	v_mov_b32_e32 v86, v248
	v_cmpx_gt_i32_e32 9, v38
	v_mov_b32_e32 v85, v248
	v_cmpx_gt_i32_e32 8, v38
	v_mov_b32_e32 v84, v248
	v_cmpx_gt_i32_e32 3, v38
	v_mov_b32_e32 v83, v248
	v_cmpx_gt_i32_e32 2, v38
	v_mov_b32_e32 v82, v248
	v_cmpx_gt_i32_e32 1, v38
	v_mov_b32_e32 v81, v248
	v_cmpx_gt_i32_e32 0, v38
	v_mov_b32_e32 v80, v248

; #define WAIT_BAR(N) asm volatile("s_waitcnt vmcnt(" #N ") lgkmcnt(0)\n\ts_barrier" ::: "memory")
; #define RESC() do { if (resc) { asm volatile("s_waitcnt lgkmcnt(0)" ::: "memory"); \
;       _Pragma("unroll") for (int d_ = 0; d_ < 2; ++d_) _Pragma("unroll") for (int r = 0; r < 16; ++r) o[d_][r] *= wsf[crow(r, hi)]; } } while (0)
; #define ROT() do { sl_prev = sl_cur; sl_cur = sl_next; sl_next = (sl_next == (NSLOT - 1) * SLOTB) ? 0 : sl_next + SLOTB; } while (0)
; template <bool MOBA, int THRL> ...
;     ...
;     int t = 1;
;     ...
;     for (; t + 5 < NT; t += 2) {
;         STEP(pB0, pB1, pA0, pA1, t, true, true, true);       WAIT_BAR(2); RESC(); ROT();
.Lmask_dead_3:
	v_mov_b32_e32 v64, 0
	v_mov_b32_e32 v81, 0
	v_mov_b32_e32 v80, 0
	v_mov_b32_e32 v65, 0
	v_mov_b32_e32 v82, 0
	v_mov_b32_e32 v66, 0
	v_mov_b32_e32 v83, 0
	v_mov_b32_e32 v67, 0
	v_mov_b32_e32 v84, 0
	v_mov_b32_e32 v68, 0
	v_mov_b32_e32 v85, 0
	v_mov_b32_e32 v69, 0
	v_mov_b32_e32 v86, 0
	v_mov_b32_e32 v70, 0
	v_mov_b32_e32 v87, 0
	v_mov_b32_e32 v71, 0
	v_mov_b32_e32 v88, 0
	v_mov_b32_e32 v72, 0
	v_mov_b32_e32 v89, 0
	v_mov_b32_e32 v73, 0
	v_mov_b32_e32 v90, 0
	v_mov_b32_e32 v74, 0
	v_mov_b32_e32 v91, 0
	v_mov_b32_e32 v75, 0
	v_mov_b32_e32 v92, 0
	v_mov_b32_e32 v76, 0
	v_mov_b32_e32 v93, 0
	v_mov_b32_e32 v77, 0
	v_mov_b32_e32 v94, 0
	v_mov_b32_e32 v78, 0
	v_mov_b32_e32 v95, 0
	v_mov_b32_e32 v79, 0
	v_add_f32_e32 v233, v197, v36
	s_mov_b64 s[40:41], 0
	s_waitcnt lgkmcnt(14)
	v_mfma_f32_32x32x16_f16 v[16:31], v[144:147], v[156:159], v[16:31]
	v_lshl_add_u32 v44, s18, 8, v232
	ds_read_b128 v[156:159], v44
	ds_read_b128 v[36:39], v44 offset:128
	s_waitcnt lgkmcnt(14)
	v_mfma_f32_32x32x16_f16 v[0:15], v[144:147], v[152:155], v[0:15]
	ds_read_b128 v[188:191], v44 offset:32
	ds_read_b128 v[198:201], v44 offset:160
	v_add_u32_e32 v144, s11, v230
	ds_read_b128 v[176:179], v144
	ds_read_b128 v[172:175], v144 offset:512
	s_waitcnt lgkmcnt(14)
	v_mfma_f32_32x32x16_f16 v[16:31], v[140:143], v[148:151], v[16:31]
	ds_read_b128 v[56:59], v44 offset:64
	ds_read_b128 v[40:43], v44 offset:192
	ds_read_b128 v[168:171], v144 offset:2048
	ds_read_b128 v[164:167], v144 offset:2560
	v_mfma_f32_32x32x16_f16 v[0:15], v[140:143], v[52:55], v[0:15]
	ds_read_b128 v[60:63], v44 offset:96
	ds_read_b128 v[44:47], v44 offset:224
	ds_read_b128 v[160:163], v144 offset:4096
	ds_read_b128 v[152:155], v144 offset:4608
	s_waitcnt lgkmcnt(14)
	v_mfma_f32_32x32x16_f16 v[16:31], v[136:139], v[48:51], v[16:31]
	s_waitcnt lgkmcnt(13)
	v_pk_add_f32 v[48:49], v[156:157], v[218:219] op_sel_hi:[1,0] neg_lo:[0,1] neg_hi:[0,1]
	v_pk_add_f32 v[50:51], v[158:159], v[218:219] op_sel_hi:[1,0] neg_lo:[0,1] neg_hi:[0,1]
	s_waitcnt lgkmcnt(11)
	v_pk_add_f32 v[52:53], v[188:189], v[218:219] op_sel_hi:[1,0] neg_lo:[0,1] neg_hi:[0,1]
	v_pk_add_f32 v[54:55], v[190:191], v[218:219] op_sel_hi:[1,0] neg_lo:[0,1] neg_hi:[0,1]
	s_waitcnt lgkmcnt(3)
	ds_read_b128 v[156:159], v144 offset:6144
	ds_read_b128 v[148:151], v144 offset:6656
	v_mfma_f32_32x32x16_f16 v[0:15], v[136:139], v[184:187], v[0:15]
	v_pk_add_f32 v[56:57], v[56:57], v[218:219] op_sel_hi:[1,0] neg_lo:[0,1] neg_hi:[0,1]
	v_pk_add_f32 v[58:59], v[58:59], v[218:219] op_sel_hi:[1,0] neg_lo:[0,1] neg_hi:[0,1]
	v_pk_add_f32 v[60:61], v[60:61], v[218:219] op_sel_hi:[1,0] neg_lo:[0,1] neg_hi:[0,1]
	v_pk_add_f32 v[62:63], v[62:63], v[218:219] op_sel_hi:[1,0] neg_lo:[0,1] neg_hi:[0,1]
	s_nop 0
	v_mfma_f32_32x32x16_f16 v[16:31], v[132:135], v[32:35], v[16:31]
	v_pk_add_f32 v[32:33], v[36:37], v[218:219] op_sel_hi:[1,0] neg_lo:[0,1] neg_hi:[0,1]
	v_pk_add_f32 v[34:35], v[38:39], v[218:219] op_sel_hi:[1,0] neg_lo:[0,1] neg_hi:[0,1]
	v_pk_add_f32 v[36:37], v[198:199], v[218:219] op_sel_hi:[1,0] neg_lo:[0,1] neg_hi:[0,1]
	v_pk_add_f32 v[38:39], v[200:201], v[218:219] op_sel_hi:[1,0] neg_lo:[0,1] neg_hi:[0,1]
	s_waitcnt lgkmcnt(4)
	v_mfma_f32_32x32x16_f16 v[0:15], v[132:135], v[180:183], v[0:15]
	v_pk_add_f32 v[40:41], v[40:41], v[218:219] op_sel_hi:[1,0] neg_lo:[0,1] neg_hi:[0,1]
	v_pk_add_f32 v[42:43], v[42:43], v[218:219] op_sel_hi:[1,0] neg_lo:[0,1] neg_hi:[0,1]
	v_pk_add_f32 v[44:45], v[44:45], v[218:219] op_sel_hi:[1,0] neg_lo:[0,1] neg_hi:[0,1]
	v_pk_add_f32 v[46:47], v[46:47], v[218:219] op_sel_hi:[1,0] neg_lo:[0,1] neg_hi:[0,1]
	s_nop 0
	s_waitcnt vmcnt(2) lgkmcnt(0)
	s_barrier
	s_andn2_b64 vcc, exec, s[40:41]
	s_branch .LBB0_635
